# custom fp8 conversion helper (73 helper WGs, split 0x40a0) + router loop: bf16 unpack of the next x block moved behind the MFMA block, counted vmcnt
# baseline (speedup 1.0000x reference)
; #define LAS __attribute__((address_space(3)))
; __device__ __forceinline__ void p0_items(const P& p, LAS unsigned char* lds, int first, int last, int gw, int NGW, int wave, int lane) {
;     LAS float* scr = (LAS float*)(lds + wave * 16384);
;     unsigned char* ws = p.ws;
;     constexpr int I_IN = P0_I_IN, I_OUT = P0_I_OUT, I_CQ = P0_I_CQ, I_CKV = P0_I_CKV, I_CO = P0_I_CO, I_G = P0_I_G, I_GU = P0_I_GU;
;     ...
;     const int it0 = first + gw, st = NGW;
;     if (it0 < last) {
;         TrItem d0, d1, d2; f32x4 v0[16], v1[16], v2[16];
;         P0_DESC(d0, it0); tr_load(d0, v0, lane); d1 = d0; d2 = d0;
;         if (it0 + st < last) { P0_DESC(d1, it0 + st); tr_load(d1, v1, lane); }
;         for (int it = it0; it < last; it += 3 * st) {
;             if (it + 2 * st < last) { P0_DESC(d2, it + 2 * st); tr_load(d2, v2, lane); }
; __global__ void __launch_bounds__(NWAVES * 64, 2) fwd(P p) {
;     ...
;     const int GP1 = (G == 256) ? G - NHELP : G, p0_last = (G == 256) ? P0_SPLIT : P0_NITEMS;
.LBB5_437:
	s_cmp_lt_i32 s24, 2
	s_cselect_b64 s[44:45], -1, 0
	s_and_b64 s[0:1], s[44:45], s[0:1]
	s_andn2_b64 vcc, exec, s[0:1]
	s_cbranch_vccnz .LBB5_819
	s_and_b64 s[0:1], s[80:81], exec
	s_cselect_b32 s27, 0xb7, s33
	s_cmp_ge_i32 s2, s27
	s_mov_b64 s[0:1], -1
	s_cbranch_scc0 .LBB5_767
	s_sub_i32 s0, s2, s27
	v_writelane_b32 v252, s44, 4
	s_lshl_b32 s0, s0, 3
	s_add_i32 s5, s3, s95
	v_writelane_b32 v252, s45, 5
	s_add_i32 s4, s5, s0
	v_writelane_b32 v252, s94, 22
	s_nop 0
	v_writelane_b32 v252, s95, 23
	v_readlane_b32 s50, v253, 50
	v_readlane_b32 s51, v253, 51
	v_readlane_b32 s12, v253, 56
	v_readlane_b32 s13, v253, 57
	v_readlane_b32 s14, v253, 4
	v_readlane_b32 s15, v253, 5
	s_sub_i32 s5, s33, s27
	s_lshl_b32 s5, s5, 3
	s_mov_b32 s6, 0x1a480
	s_mov_b32 s62, 1
	s_lshl_b32 s59, s5, 1
	s_add_i32 s60, s59, s5
	s_lshl_b32 s61, s5, 2
	s_add_u32 s16, s22, 0x8000000
	s_addc_u32 s17, s23, 0
	s_add_u32 s18, s22, 0x28000000
	s_addc_u32 s19, s23, 0
	s_lshl_b32 s58, s95, 14
	v_lshlrev_b32_e32 v1, 4, v0
	global_load_dwordx4 v[4:7], v1, s[50:51]
	v_and_b32_e32 v2, 7, v0
	v_bfe_u32 v3, v0, 3, 3
	v_lshlrev_b32_e32 v200, 4, v2
	v_lshl_add_u32 v201, v3, 13, v200
	v_lshl_add_u32 v200, v3, 14, v200
	v_lshlrev_b32_e32 v202, 6, v2
	v_lshl_add_u32 v211, v3, 7, s58
	v_xor_b32_e32 v242, 0, v2
	v_lshl_add_u32 v203, v242, 4, v211
	v_xor_b32_e32 v242, 1, v2
	v_lshl_add_u32 v204, v242, 4, v211
	v_xor_b32_e32 v242, 2, v2
	v_lshl_add_u32 v205, v242, 4, v211
	v_xor_b32_e32 v242, 3, v2
	v_lshl_add_u32 v206, v242, 4, v211
	v_xor_b32_e32 v242, 4, v2
	v_lshl_add_u32 v207, v242, 4, v211
	v_xor_b32_e32 v242, 5, v2
	v_lshl_add_u32 v208, v242, 4, v211
	v_xor_b32_e32 v242, 6, v2
	v_lshl_add_u32 v209, v242, 4, v211
	v_xor_b32_e32 v242, 7, v2
	v_lshl_add_u32 v210, v242, 4, v211
	v_lshl_add_u32 v211, v2, 11, s58
	v_and_b32_e32 v242, 3, v3
	v_lshl_add_u32 v211, v242, 2, v211
	v_lshrrev_b32_e32 v243, 2, v3
	v_add_u32_e32 v242, 0, v243
	v_xor_b32_e32 v242, v242, v2
	v_lshl_add_u32 v230, v242, 4, v211
	v_add_u32_e32 v234, 0x400, v230
	v_add_u32_e32 v242, 2, v243
	v_xor_b32_e32 v242, v242, v2
	v_lshl_add_u32 v231, v242, 4, v211
	v_add_u32_e32 v235, 0x400, v231
	v_add_u32_e32 v242, 4, v243
	v_xor_b32_e32 v242, v242, v2
	v_lshl_add_u32 v232, v242, 4, v211
	v_add_u32_e32 v236, 0x400, v232
	v_add_u32_e32 v242, 6, v243
	v_xor_b32_e32 v242, v242, v2
	v_lshl_add_u32 v233, v242, 4, v211
	v_add_u32_e32 v237, 0x400, v233
	v_lshlrev_b32_e32 v242, 4, v2
	v_lshl_add_u32 v238, v3, 11, v242
	v_add_u32_e32 v239, 0x4000, v238
	v_add_u32_e32 v240, 0x8000, v238
	v_add_u32_e32 v241, 0xc000, v238
	s_waitcnt vmcnt(0)
	v_mul_f32_e32 v4, 0x42800000, v4
	v_mul_f32_e32 v5, 0x42800000, v5
	v_mul_f32_e32 v6, 0x42800000, v6
	v_mul_f32_e32 v7, 0x42800000, v7
	v_add_u32_e32 v2, 0x21800, v1
	ds_write_b128 v2, v[4:7]
	v_and_b32_e32 v2, 48, v1
	v_add_u32_e32 v2, 0x23800, v2
	v_mov_b32_e32 v8, 0x42800000
	v_mov_b32_e32 v9, 0x42800000
	v_mov_b32_e32 v10, 0x42800000
	v_mov_b32_e32 v11, 0x42800000
	ds_write_b128 v2, v[8:11]
	s_waitcnt lgkmcnt(0)
	s_barrier
	s_cmp_lt_u32 s4, s6
	s_cbranch_scc0 .Lhlp_done
	s_sub_i32 s50, s4, 0x2480
	s_cmp_lt_u32 s50, 0x10000
	s_cbranch_scc0 .Lhlp_dn_p0
	s_lshr_b32 s51, s50, 11
	s_bfe_u32 s52, s50, 0x40007
	s_and_b32 s53, s50, 0x7f
	s_lshl_b32 s54, s53, 5
	s_lshl_b32 s55, s51, 25
	s_lshl_b32 s56, s52, 21
	s_add_u32 s55, s55, s56
	s_lshl_b32 s56, s54, 2
	s_add_u32 s55, s55, s56
	s_add_u32 s8, s12, s55
	s_addc_u32 s9, s13, 0
	s_mov_b32 s10, 0x20000
	s_bfe_u32 s56, s53, 0x40002
	s_lshl_b32 s56, s56, 8
	s_and_b32 s57, s53, 3
	s_lshl_b32 s57, s57, 5
	s_add_u32 s56, s56, s57
	s_lshr_b32 s57, s53, 6
	s_lshl_b32 s57, s57, 7
	s_add_u32 s56, s56, s57
	s_lshl_b32 s56, s56, 11
	s_lshl_b32 s57, s51, 23
	s_add_u32 s56, s56, s57
	s_lshl_b32 s57, s52, 7
	s_add_u32 s56, s56, s57
	s_add_u32 s34, s16, s56
	s_addc_u32 s35, s17, 0
	s_lshl_b32 s57, s52, 9
	s_add_u32 s36, s57, 0x21800
	s_mov_b32 s37, -1
	v_mov_b32_e32 v211, v200
	s_branch .Lhlp_ld_p0

; #define GAS __attribute__((address_space(1)))
; #define LAS __attribute__((address_space(3)))
; __device__ __forceinline__ unsigned pk4_fp8(float a, float b, float c, float d) { int w = 0; w = __builtin_amdgcn_cvt_pk_fp8_f32(a, b, w, false); w = __builtin_amdgcn_cvt_pk_fp8_f32(c, d, w, true); return (unsigned)w; }
; #define LDS_WAIT() asm volatile("s_waitcnt lgkmcnt(0)" ::: "memory")
; __device__ __forceinline__ void tr_finish(const TrItem& d, const f32x4 (&v)[16], LAS float* scr, int lane_) {
;     int lane = lane_; asm volatile("" : "+v"(lane));
;     const int c = lane & 7;
;     if (d.is8) {
;         { const int g = lane & 7, r0 = lane >> 3;
; #pragma unroll
;           for (int i = 0; i < 16; ++i) { const float gs = (d.gain ? d.gain[d.k0 + r0 + 8 * i] : 1.0f) * W8_SCALE; *(LAS f32x4*)(scr + (r0 + 8 * i) * 32 + ((g ^ (i >> 1)) << 2)) = v[i] * gs;
;               if ((i & 3) == 3) asm volatile("" ::: "memory"); } }
;         LDS_WAIT(); asm volatile("" ::: "memory");
; #pragma unroll
;         for (int j = 0; j < 4; ++j) { const int n = (lane >> 3) + 8 * j; const LAS float* s = scr + (16 * c) * 32 + ((((n >> 2) ^ c) << 2) + (n & 3));
;             v4u o; o.x = pk4_fp8(s[0 * 32], s[1 * 32], s[2 * 32], s[3 * 32]); o.y = pk4_fp8(s[4 * 32], s[5 * 32], s[6 * 32], s[7 * 32]); o.z = pk4_fp8(s[8 * 32], s[9 * 32], s[10 * 32], s[11 * 32]); o.w = pk4_fp8(s[12 * 32], s[13 * 32], s[14 * 32], s[15 * 32]);
;             __builtin_nontemporal_store(o, (GAS v4u*)(d.WT + (size_t)(d.drow0 + n) * d.K + d.k0 + 16 * c)); }
; __device__ __forceinline__ void p0_items(const P& p, LAS unsigned char* lds, int first, int last, int gw, int NGW, int wave, int lane) {
;     ...
;         for (int it = it0; it < last; it += 3 * st) {
;             if (it + 2 * st < last) { P0_DESC(d2, it + 2 * st); tr_load(d2, v2, lane); }
;             tr_finish(d0, v0, scr, lane);
;             if (it + st >= last) break;
.Lhlp_fin_0:
	s_cmp_eq_u32 s62, 0
	s_cbranch_scc1 .Lhlp_st_0
	s_waitcnt vmcnt(32)
.Lhlp_st_0:
	s_waitcnt vmcnt(40)
	ds_write_b128 v203, v[4:7]
	ds_write_b128 v203, v[8:11] offset:1024
	ds_write_b128 v204, v[12:15] offset:2048
	ds_write_b128 v204, v[16:19] offset:3072
	ds_write_b128 v205, v[20:23] offset:4096
	ds_write_b128 v205, v[24:27] offset:5120
	ds_write_b128 v206, v[28:31] offset:6144
	ds_write_b128 v206, v[32:35] offset:7168
	ds_write_b128 v207, v[36:39] offset:8192
	ds_write_b128 v207, v[40:43] offset:9216
	ds_write_b128 v208, v[44:47] offset:10240
	ds_write_b128 v208, v[48:51] offset:11264
	ds_write_b128 v209, v[52:55] offset:12288
	ds_write_b128 v209, v[56:59] offset:13312
	ds_write_b128 v210, v[60:63] offset:14336
	ds_write_b128 v210, v[64:67] offset:15360
	v_and_b32_e32 v242, s37, v202
	v_add_u32_e32 v242, s36, v242
	s_waitcnt lgkmcnt(0)
	ds_read_b128 v[214:217], v242
	ds_read_b128 v[218:221], v242 offset:16
	ds_read_b128 v[222:225], v242 offset:32
	ds_read_b128 v[226:229], v242 offset:48
	ds_read2_b32 v[4:5], v230 offset1:32
	ds_read2_b32 v[6:7], v230 offset0:64 offset1:96
	ds_read2_b32 v[8:9], v230 offset0:128 offset1:160
	ds_read2_b32 v[10:11], v230 offset0:192 offset1:224
	ds_read2_b32 v[12:13], v234 offset1:32
	ds_read2_b32 v[14:15], v234 offset0:64 offset1:96
	ds_read2_b32 v[16:17], v234 offset0:128 offset1:160
	ds_read2_b32 v[18:19], v234 offset0:192 offset1:224
	s_waitcnt lgkmcnt(0)
	ds_read2_b32 v[20:21], v231 offset1:32
	ds_read2_b32 v[22:23], v231 offset0:64 offset1:96
	ds_read2_b32 v[24:25], v231 offset0:128 offset1:160
	ds_read2_b32 v[26:27], v231 offset0:192 offset1:224
	ds_read2_b32 v[28:29], v235 offset1:32
	ds_read2_b32 v[30:31], v235 offset0:64 offset1:96
	ds_read2_b32 v[32:33], v235 offset0:128 offset1:160
	ds_read2_b32 v[34:35], v235 offset0:192 offset1:224
	v_pk_mul_f32 v[4:5], v[4:5], v[214:215]
	v_pk_mul_f32 v[6:7], v[6:7], v[216:217]
	v_pk_mul_f32 v[8:9], v[8:9], v[218:219]
	v_pk_mul_f32 v[10:11], v[10:11], v[220:221]
	v_pk_mul_f32 v[12:13], v[12:13], v[222:223]
	v_pk_mul_f32 v[14:15], v[14:15], v[224:225]
	v_pk_mul_f32 v[16:17], v[16:17], v[226:227]
	v_pk_mul_f32 v[18:19], v[18:19], v[228:229]
	v_cvt_pk_fp8_f32 v244, v4, v5
	v_cvt_pk_fp8_f32 v245, v8, v9
	v_cvt_pk_fp8_f32 v246, v12, v13
	v_cvt_pk_fp8_f32 v247, v16, v17
	v_cvt_pk_fp8_f32 v244, v6, v7 op_sel:[0,0,1]
	v_cvt_pk_fp8_f32 v245, v10, v11 op_sel:[0,0,1]
	v_cvt_pk_fp8_f32 v246, v14, v15 op_sel:[0,0,1]
	v_cvt_pk_fp8_f32 v247, v18, v19 op_sel:[0,0,1]
	s_nop 0
	global_store_dwordx4 v238, v[244:247], s[34:35] nt
	s_waitcnt lgkmcnt(0)
	ds_read2_b32 v[36:37], v232 offset1:32
	ds_read2_b32 v[38:39], v232 offset0:64 offset1:96
	ds_read2_b32 v[40:41], v232 offset0:128 offset1:160
	ds_read2_b32 v[42:43], v232 offset0:192 offset1:224
	ds_read2_b32 v[44:45], v236 offset1:32
	ds_read2_b32 v[46:47], v236 offset0:64 offset1:96
	ds_read2_b32 v[48:49], v236 offset0:128 offset1:160
	ds_read2_b32 v[50:51], v236 offset0:192 offset1:224
	v_pk_mul_f32 v[20:21], v[20:21], v[214:215]
	v_pk_mul_f32 v[22:23], v[22:23], v[216:217]
	v_pk_mul_f32 v[24:25], v[24:25], v[218:219]
	v_pk_mul_f32 v[26:27], v[26:27], v[220:221]
	v_pk_mul_f32 v[28:29], v[28:29], v[222:223]
	v_pk_mul_f32 v[30:31], v[30:31], v[224:225]
	v_pk_mul_f32 v[32:33], v[32:33], v[226:227]
	v_pk_mul_f32 v[34:35], v[34:35], v[228:229]
	v_cvt_pk_fp8_f32 v244, v20, v21
	v_cvt_pk_fp8_f32 v245, v24, v25
	v_cvt_pk_fp8_f32 v246, v28, v29
	v_cvt_pk_fp8_f32 v247, v32, v33
	v_cvt_pk_fp8_f32 v244, v22, v23 op_sel:[0,0,1]
	v_cvt_pk_fp8_f32 v245, v26, v27 op_sel:[0,0,1]
	v_cvt_pk_fp8_f32 v246, v30, v31 op_sel:[0,0,1]
	v_cvt_pk_fp8_f32 v247, v34, v35 op_sel:[0,0,1]
	s_nop 0
	global_store_dwordx4 v239, v[244:247], s[34:35] nt
	s_waitcnt lgkmcnt(0)
	ds_read2_b32 v[52:53], v233 offset1:32
	ds_read2_b32 v[54:55], v233 offset0:64 offset1:96
	ds_read2_b32 v[56:57], v233 offset0:128 offset1:160
	ds_read2_b32 v[58:59], v233 offset0:192 offset1:224
	ds_read2_b32 v[60:61], v237 offset1:32
	ds_read2_b32 v[62:63], v237 offset0:64 offset1:96
	ds_read2_b32 v[64:65], v237 offset0:128 offset1:160
	ds_read2_b32 v[66:67], v237 offset0:192 offset1:224
	v_pk_mul_f32 v[36:37], v[36:37], v[214:215]
	v_pk_mul_f32 v[38:39], v[38:39], v[216:217]
	v_pk_mul_f32 v[40:41], v[40:41], v[218:219]
	v_pk_mul_f32 v[42:43], v[42:43], v[220:221]
	v_pk_mul_f32 v[44:45], v[44:45], v[222:223]
	v_pk_mul_f32 v[46:47], v[46:47], v[224:225]
	v_pk_mul_f32 v[48:49], v[48:49], v[226:227]
	v_pk_mul_f32 v[50:51], v[50:51], v[228:229]
	v_cvt_pk_fp8_f32 v244, v36, v37
	v_cvt_pk_fp8_f32 v245, v40, v41
	v_cvt_pk_fp8_f32 v246, v44, v45
	v_cvt_pk_fp8_f32 v247, v48, v49
	v_cvt_pk_fp8_f32 v244, v38, v39 op_sel:[0,0,1]
	v_cvt_pk_fp8_f32 v245, v42, v43 op_sel:[0,0,1]
	v_cvt_pk_fp8_f32 v246, v46, v47 op_sel:[0,0,1]
	v_cvt_pk_fp8_f32 v247, v50, v51 op_sel:[0,0,1]
	s_nop 0
	global_store_dwordx4 v240, v[244:247], s[34:35] nt
	s_waitcnt lgkmcnt(0)
	v_pk_mul_f32 v[52:53], v[52:53], v[214:215]
	v_pk_mul_f32 v[54:55], v[54:55], v[216:217]
	v_pk_mul_f32 v[56:57], v[56:57], v[218:219]
	v_pk_mul_f32 v[58:59], v[58:59], v[220:221]
	v_pk_mul_f32 v[60:61], v[60:61], v[222:223]
	v_pk_mul_f32 v[62:63], v[62:63], v[224:225]
	v_pk_mul_f32 v[64:65], v[64:65], v[226:227]
	v_pk_mul_f32 v[66:67], v[66:67], v[228:229]
	v_cvt_pk_fp8_f32 v244, v52, v53
	v_cvt_pk_fp8_f32 v245, v56, v57
	v_cvt_pk_fp8_f32 v246, v60, v61
	v_cvt_pk_fp8_f32 v247, v64, v65
	v_cvt_pk_fp8_f32 v244, v54, v55 op_sel:[0,0,1]
	v_cvt_pk_fp8_f32 v245, v58, v59 op_sel:[0,0,1]
	v_cvt_pk_fp8_f32 v246, v62, v63 op_sel:[0,0,1]
	v_cvt_pk_fp8_f32 v247, v66, v67 op_sel:[0,0,1]
	s_nop 0
	global_store_dwordx4 v241, v[244:247], s[34:35] nt
	s_add_i32 s7, s4, s5
	s_cmp_lt_u32 s7, s6
	s_cbranch_scc0 .Lhlp_done
	s_add_i32 s7, s4, s60
	s_cmp_lt_u32 s7, s6
	s_cbranch_scc0 .Lhlp_skip_1
	s_sub_i32 s50, s7, 0x2480
	s_cmp_lt_u32 s50, 0x10000
	s_cbranch_scc0 .Lhlp_dn_k1
	s_lshr_b32 s51, s50, 11
	s_bfe_u32 s52, s50, 0x40007
	s_and_b32 s53, s50, 0x7f
	s_lshl_b32 s54, s53, 5
	s_lshl_b32 s55, s51, 25
	s_lshl_b32 s56, s52, 21
	s_add_u32 s55, s55, s56
	s_lshl_b32 s56, s54, 2
	s_add_u32 s55, s55, s56
	s_add_u32 s8, s12, s55
	s_addc_u32 s9, s13, 0
	s_mov_b32 s10, 0x20000
	s_bfe_u32 s56, s53, 0x40002
	s_lshl_b32 s56, s56, 8
	s_and_b32 s57, s53, 3
	s_lshl_b32 s57, s57, 5
	s_add_u32 s56, s56, s57
	s_lshr_b32 s57, s53, 6
	s_lshl_b32 s57, s57, 7
	s_add_u32 s56, s56, s57
	s_lshl_b32 s56, s56, 11
	s_lshl_b32 s57, s51, 23
	s_add_u32 s56, s56, s57
	s_lshl_b32 s57, s52, 7
	s_add_u32 s56, s56, s57
	s_add_u32 s34, s16, s56
	s_addc_u32 s35, s17, 0
	s_lshl_b32 s57, s52, 9
	s_add_u32 s36, s57, 0x21800
	s_mov_b32 s37, -1
	v_mov_b32_e32 v211, v200
	s_branch .Lhlp_ld_k1

; #define GAS __attribute__((address_space(1)))
; #define LAS __attribute__((address_space(3)))
; __device__ __forceinline__ unsigned pk4_fp8(float a, float b, float c, float d) { int w = 0; w = __builtin_amdgcn_cvt_pk_fp8_f32(a, b, w, false); w = __builtin_amdgcn_cvt_pk_fp8_f32(c, d, w, true); return (unsigned)w; }
; __device__ __forceinline__ void tr_finish(const TrItem& d, const f32x4 (&v)[16], LAS float* scr, int lane_) {
;     ...
;     if (d.is8) {
;         { const int g = lane & 7, r0 = lane >> 3;
; #pragma unroll
;           for (int i = 0; i < 16; ++i) { const float gs = (d.gain ? d.gain[d.k0 + r0 + 8 * i] : 1.0f) * W8_SCALE; *(LAS f32x4*)(scr + (r0 + 8 * i) * 32 + ((g ^ (i >> 1)) << 2)) = v[i] * gs;
;               if ((i & 3) == 3) asm volatile("" ::: "memory"); } }
;         LDS_WAIT(); asm volatile("" ::: "memory");
; #pragma unroll
;         for (int j = 0; j < 4; ++j) { const int n = (lane >> 3) + 8 * j; const LAS float* s = scr + (16 * c) * 32 + ((((n >> 2) ^ c) << 2) + (n & 3));
;             v4u o; o.x = pk4_fp8(s[0 * 32], s[1 * 32], s[2 * 32], s[3 * 32]); o.y = pk4_fp8(s[4 * 32], s[5 * 32], s[6 * 32], s[7 * 32]); o.z = pk4_fp8(s[8 * 32], s[9 * 32], s[10 * 32], s[11 * 32]); o.w = pk4_fp8(s[12 * 32], s[13 * 32], s[14 * 32], s[15 * 32]);
;             __builtin_nontemporal_store(o, (GAS v4u*)(d.WT + (size_t)(d.drow0 + n) * d.K + d.k0 + 16 * c)); }
; __device__ __forceinline__ void p0_items(const P& p, LAS unsigned char* lds, int first, int last, int gw, int NGW, int wave, int lane) {
;     ...
;     const int it0 = first + gw, st = NGW;
;     if (it0 < last) {
;         TrItem d0, d1, d2; f32x4 v0[16], v1[16], v2[16];
;         P0_DESC(d0, it0); tr_load(d0, v0, lane); d1 = d0; d2 = d0;
;         if (it0 + st < last) { P0_DESC(d1, it0 + st); tr_load(d1, v1, lane); }
;         for (int it = it0; it < last; it += 3 * st) {
;             if (it + 2 * st < last) { P0_DESC(d2, it + 2 * st); tr_load(d2, v2, lane); }
;             tr_finish(d0, v0, scr, lane);
;             if (it + st >= last) break;
;             if (it + 3 * st < last) { P0_DESC(d0, it + 3 * st); tr_load(d0, v0, lane); }
;             tr_finish(d1, v1, scr, lane);
;             if (it + 2 * st >= last) break;
;             if (it + 4 * st < last) { P0_DESC(d1, it + 4 * st); tr_load(d1, v1, lane); }
;             tr_finish(d2, v2, scr, lane);
.Lhlp_fin_1:
	s_cmp_eq_u32 s62, 0
	s_cbranch_scc1 .Lhlp_st_1
	s_waitcnt vmcnt(36)
.Lhlp_st_1:
	s_waitcnt vmcnt(40)
	ds_write_b128 v203, v[68:71]
	ds_write_b128 v203, v[72:75] offset:1024
	ds_write_b128 v204, v[76:79] offset:2048
	ds_write_b128 v204, v[80:83] offset:3072
	ds_write_b128 v205, v[84:87] offset:4096
	ds_write_b128 v205, v[88:91] offset:5120
	ds_write_b128 v206, v[92:95] offset:6144
	ds_write_b128 v206, v[96:99] offset:7168
	ds_write_b128 v207, v[100:103] offset:8192
	ds_write_b128 v207, v[104:107] offset:9216
	ds_write_b128 v208, v[108:111] offset:10240
	ds_write_b128 v208, v[112:115] offset:11264
	ds_write_b128 v209, v[116:119] offset:12288
	ds_write_b128 v209, v[120:123] offset:13312
	ds_write_b128 v210, v[124:127] offset:14336
	ds_write_b128 v210, v[128:131] offset:15360
	v_and_b32_e32 v242, s41, v202
	v_add_u32_e32 v242, s40, v242
	s_waitcnt lgkmcnt(0)
	ds_read_b128 v[214:217], v242
	ds_read_b128 v[218:221], v242 offset:16
	ds_read_b128 v[222:225], v242 offset:32
	ds_read_b128 v[226:229], v242 offset:48
	ds_read2_b32 v[68:69], v230 offset1:32
	ds_read2_b32 v[70:71], v230 offset0:64 offset1:96
	ds_read2_b32 v[72:73], v230 offset0:128 offset1:160
	ds_read2_b32 v[74:75], v230 offset0:192 offset1:224
	ds_read2_b32 v[76:77], v234 offset1:32
	ds_read2_b32 v[78:79], v234 offset0:64 offset1:96
	ds_read2_b32 v[80:81], v234 offset0:128 offset1:160
	ds_read2_b32 v[82:83], v234 offset0:192 offset1:224
	s_waitcnt lgkmcnt(0)
	ds_read2_b32 v[84:85], v231 offset1:32
	ds_read2_b32 v[86:87], v231 offset0:64 offset1:96
	ds_read2_b32 v[88:89], v231 offset0:128 offset1:160
	ds_read2_b32 v[90:91], v231 offset0:192 offset1:224
	ds_read2_b32 v[92:93], v235 offset1:32
	ds_read2_b32 v[94:95], v235 offset0:64 offset1:96
	ds_read2_b32 v[96:97], v235 offset0:128 offset1:160
	ds_read2_b32 v[98:99], v235 offset0:192 offset1:224
	v_pk_mul_f32 v[68:69], v[68:69], v[214:215]
	v_pk_mul_f32 v[70:71], v[70:71], v[216:217]
	v_pk_mul_f32 v[72:73], v[72:73], v[218:219]
	v_pk_mul_f32 v[74:75], v[74:75], v[220:221]
	v_pk_mul_f32 v[76:77], v[76:77], v[222:223]
	v_pk_mul_f32 v[78:79], v[78:79], v[224:225]
	v_pk_mul_f32 v[80:81], v[80:81], v[226:227]
	v_pk_mul_f32 v[82:83], v[82:83], v[228:229]
	v_cvt_pk_fp8_f32 v244, v68, v69
	v_cvt_pk_fp8_f32 v245, v72, v73
	v_cvt_pk_fp8_f32 v246, v76, v77
	v_cvt_pk_fp8_f32 v247, v80, v81
	v_cvt_pk_fp8_f32 v244, v70, v71 op_sel:[0,0,1]
	v_cvt_pk_fp8_f32 v245, v74, v75 op_sel:[0,0,1]
	v_cvt_pk_fp8_f32 v246, v78, v79 op_sel:[0,0,1]
	v_cvt_pk_fp8_f32 v247, v82, v83 op_sel:[0,0,1]
	s_nop 0
	global_store_dwordx4 v238, v[244:247], s[38:39] nt
	s_waitcnt lgkmcnt(0)
	ds_read2_b32 v[100:101], v232 offset1:32
	ds_read2_b32 v[102:103], v232 offset0:64 offset1:96
	ds_read2_b32 v[104:105], v232 offset0:128 offset1:160
	ds_read2_b32 v[106:107], v232 offset0:192 offset1:224
	ds_read2_b32 v[108:109], v236 offset1:32
	ds_read2_b32 v[110:111], v236 offset0:64 offset1:96
	ds_read2_b32 v[112:113], v236 offset0:128 offset1:160
	ds_read2_b32 v[114:115], v236 offset0:192 offset1:224
	v_pk_mul_f32 v[84:85], v[84:85], v[214:215]
	v_pk_mul_f32 v[86:87], v[86:87], v[216:217]
	v_pk_mul_f32 v[88:89], v[88:89], v[218:219]
	v_pk_mul_f32 v[90:91], v[90:91], v[220:221]
	v_pk_mul_f32 v[92:93], v[92:93], v[222:223]
	v_pk_mul_f32 v[94:95], v[94:95], v[224:225]
	v_pk_mul_f32 v[96:97], v[96:97], v[226:227]
	v_pk_mul_f32 v[98:99], v[98:99], v[228:229]
	v_cvt_pk_fp8_f32 v244, v84, v85
	v_cvt_pk_fp8_f32 v245, v88, v89
	v_cvt_pk_fp8_f32 v246, v92, v93
	v_cvt_pk_fp8_f32 v247, v96, v97
	v_cvt_pk_fp8_f32 v244, v86, v87 op_sel:[0,0,1]
	v_cvt_pk_fp8_f32 v245, v90, v91 op_sel:[0,0,1]
	v_cvt_pk_fp8_f32 v246, v94, v95 op_sel:[0,0,1]
	v_cvt_pk_fp8_f32 v247, v98, v99 op_sel:[0,0,1]
	s_nop 0
	global_store_dwordx4 v239, v[244:247], s[38:39] nt
	s_waitcnt lgkmcnt(0)
	ds_read2_b32 v[116:117], v233 offset1:32
	ds_read2_b32 v[118:119], v233 offset0:64 offset1:96
	ds_read2_b32 v[120:121], v233 offset0:128 offset1:160
	ds_read2_b32 v[122:123], v233 offset0:192 offset1:224
	ds_read2_b32 v[124:125], v237 offset1:32
	ds_read2_b32 v[126:127], v237 offset0:64 offset1:96
	ds_read2_b32 v[128:129], v237 offset0:128 offset1:160
	ds_read2_b32 v[130:131], v237 offset0:192 offset1:224
	v_pk_mul_f32 v[100:101], v[100:101], v[214:215]
	v_pk_mul_f32 v[102:103], v[102:103], v[216:217]
	v_pk_mul_f32 v[104:105], v[104:105], v[218:219]
	v_pk_mul_f32 v[106:107], v[106:107], v[220:221]
	v_pk_mul_f32 v[108:109], v[108:109], v[222:223]
	v_pk_mul_f32 v[110:111], v[110:111], v[224:225]
	v_pk_mul_f32 v[112:113], v[112:113], v[226:227]
	v_pk_mul_f32 v[114:115], v[114:115], v[228:229]
	v_cvt_pk_fp8_f32 v244, v100, v101
	v_cvt_pk_fp8_f32 v245, v104, v105
	v_cvt_pk_fp8_f32 v246, v108, v109
	v_cvt_pk_fp8_f32 v247, v112, v113
	v_cvt_pk_fp8_f32 v244, v102, v103 op_sel:[0,0,1]
	v_cvt_pk_fp8_f32 v245, v106, v107 op_sel:[0,0,1]
	v_cvt_pk_fp8_f32 v246, v110, v111 op_sel:[0,0,1]
	v_cvt_pk_fp8_f32 v247, v114, v115 op_sel:[0,0,1]
	s_nop 0
	global_store_dwordx4 v240, v[244:247], s[38:39] nt
	s_waitcnt lgkmcnt(0)
	v_pk_mul_f32 v[116:117], v[116:117], v[214:215]
	v_pk_mul_f32 v[118:119], v[118:119], v[216:217]
	v_pk_mul_f32 v[120:121], v[120:121], v[218:219]
	v_pk_mul_f32 v[122:123], v[122:123], v[220:221]
	v_pk_mul_f32 v[124:125], v[124:125], v[222:223]
	v_pk_mul_f32 v[126:127], v[126:127], v[224:225]
	v_pk_mul_f32 v[128:129], v[128:129], v[226:227]
	v_pk_mul_f32 v[130:131], v[130:131], v[228:229]
	v_cvt_pk_fp8_f32 v244, v116, v117
	v_cvt_pk_fp8_f32 v245, v120, v121
	v_cvt_pk_fp8_f32 v246, v124, v125
	v_cvt_pk_fp8_f32 v247, v128, v129
	v_cvt_pk_fp8_f32 v244, v118, v119 op_sel:[0,0,1]
	v_cvt_pk_fp8_f32 v245, v122, v123 op_sel:[0,0,1]
	v_cvt_pk_fp8_f32 v246, v126, v127 op_sel:[0,0,1]
	v_cvt_pk_fp8_f32 v247, v130, v131 op_sel:[0,0,1]
	s_nop 0
	global_store_dwordx4 v241, v[244:247], s[38:39] nt
	s_add_i32 s7, s4, s59
	s_cmp_lt_u32 s7, s6
	s_cbranch_scc0 .Lhlp_done
	s_add_i32 s7, s4, s61
	s_cmp_lt_u32 s7, s6
	s_cbranch_scc0 .Lhlp_skip_2
	s_sub_i32 s50, s7, 0x2480
	s_cmp_lt_u32 s50, 0x10000
	s_cbranch_scc0 .Lhlp_dn_k2
	s_lshr_b32 s51, s50, 11
	s_bfe_u32 s52, s50, 0x40007
	s_and_b32 s53, s50, 0x7f
	s_lshl_b32 s54, s53, 5
	s_lshl_b32 s55, s51, 25
	s_lshl_b32 s56, s52, 21
	s_add_u32 s55, s55, s56
	s_lshl_b32 s56, s54, 2
	s_add_u32 s55, s55, s56
	s_add_u32 s8, s12, s55
	s_addc_u32 s9, s13, 0
	s_mov_b32 s10, 0x20000
	s_bfe_u32 s56, s53, 0x40002
	s_lshl_b32 s56, s56, 8
	s_and_b32 s57, s53, 3
	s_lshl_b32 s57, s57, 5
	s_add_u32 s56, s56, s57
	s_lshr_b32 s57, s53, 6
	s_lshl_b32 s57, s57, 7
	s_add_u32 s56, s56, s57
	s_lshl_b32 s56, s56, 11
	s_lshl_b32 s57, s51, 23
	s_add_u32 s56, s56, s57
	s_lshl_b32 s57, s52, 7
	s_add_u32 s56, s56, s57
	s_add_u32 s38, s16, s56
	s_addc_u32 s39, s17, 0
	s_lshl_b32 s57, s52, 9
	s_add_u32 s40, s57, 0x21800
	s_mov_b32 s41, -1
	v_mov_b32_e32 v211, v200
	s_branch .Lhlp_ld_k2

; #define GAS __attribute__((address_space(1)))
; #define LAS __attribute__((address_space(3)))
; __device__ __forceinline__ unsigned pk4_fp8(float a, float b, float c, float d) { int w = 0; w = __builtin_amdgcn_cvt_pk_fp8_f32(a, b, w, false); w = __builtin_amdgcn_cvt_pk_fp8_f32(c, d, w, true); return (unsigned)w; }
; #define LDS_WAIT() asm volatile("s_waitcnt lgkmcnt(0)" ::: "memory")
; __device__ __forceinline__ void tr_finish(const TrItem& d, const f32x4 (&v)[16], LAS float* scr, int lane_) {
;     ...
;     if (d.is8) {
;         { const int g = lane & 7, r0 = lane >> 3;
; #pragma unroll
;           for (int i = 0; i < 16; ++i) { const float gs = (d.gain ? d.gain[d.k0 + r0 + 8 * i] : 1.0f) * W8_SCALE; *(LAS f32x4*)(scr + (r0 + 8 * i) * 32 + ((g ^ (i >> 1)) << 2)) = v[i] * gs;
;               if ((i & 3) == 3) asm volatile("" ::: "memory"); } }
;         LDS_WAIT(); asm volatile("" ::: "memory");
; #pragma unroll
;         for (int j = 0; j < 4; ++j) { const int n = (lane >> 3) + 8 * j; const LAS float* s = scr + (16 * c) * 32 + ((((n >> 2) ^ c) << 2) + (n & 3));
;             v4u o; o.x = pk4_fp8(s[0 * 32], s[1 * 32], s[2 * 32], s[3 * 32]); o.y = pk4_fp8(s[4 * 32], s[5 * 32], s[6 * 32], s[7 * 32]); o.z = pk4_fp8(s[8 * 32], s[9 * 32], s[10 * 32], s[11 * 32]); o.w = pk4_fp8(s[12 * 32], s[13 * 32], s[14 * 32], s[15 * 32]);
;             __builtin_nontemporal_store(o, (GAS v4u*)(d.WT + (size_t)(d.drow0 + n) * d.K + d.k0 + 16 * c)); }
; __device__ __forceinline__ void p0_items(const P& p, LAS unsigned char* lds, int first, int last, int gw, int NGW, int wave, int lane) {
;     ...
;         for (int it = it0; it < last; it += 3 * st) {
;             if (it + 2 * st < last) { P0_DESC(d2, it + 2 * st); tr_load(d2, v2, lane); }
;             tr_finish(d0, v0, scr, lane);
;             if (it + st >= last) break;
;             if (it + 3 * st < last) { P0_DESC(d0, it + 3 * st); tr_load(d0, v0, lane); }
;             tr_finish(d1, v1, scr, lane);
;             if (it + 2 * st >= last) break;
;             if (it + 4 * st < last) { P0_DESC(d1, it + 4 * st); tr_load(d1, v1, lane); }
;             tr_finish(d2, v2, scr, lane);
;         }
.Lhlp_fin_2:
	s_waitcnt vmcnt(40)
	ds_write_b128 v203, v[132:135]
	ds_write_b128 v203, v[136:139] offset:1024
	ds_write_b128 v204, v[140:143] offset:2048
	ds_write_b128 v204, v[144:147] offset:3072
	ds_write_b128 v205, v[148:151] offset:4096
	ds_write_b128 v205, v[152:155] offset:5120
	ds_write_b128 v206, v[156:159] offset:6144
	ds_write_b128 v206, v[160:163] offset:7168
	ds_write_b128 v207, v[164:167] offset:8192
	ds_write_b128 v207, v[168:171] offset:9216
	ds_write_b128 v208, v[172:175] offset:10240
	ds_write_b128 v208, v[176:179] offset:11264
	ds_write_b128 v209, v[180:183] offset:12288
	ds_write_b128 v209, v[184:187] offset:13312
	ds_write_b128 v210, v[188:191] offset:14336
	ds_write_b128 v210, v[192:195] offset:15360
	v_and_b32_e32 v242, s49, v202
	v_add_u32_e32 v242, s48, v242
	s_waitcnt lgkmcnt(0)
	ds_read_b128 v[214:217], v242
	ds_read_b128 v[218:221], v242 offset:16
	ds_read_b128 v[222:225], v242 offset:32
	ds_read_b128 v[226:229], v242 offset:48
	ds_read2_b32 v[132:133], v230 offset1:32
	ds_read2_b32 v[134:135], v230 offset0:64 offset1:96
	ds_read2_b32 v[136:137], v230 offset0:128 offset1:160
	ds_read2_b32 v[138:139], v230 offset0:192 offset1:224
	ds_read2_b32 v[140:141], v234 offset1:32
	ds_read2_b32 v[142:143], v234 offset0:64 offset1:96
	ds_read2_b32 v[144:145], v234 offset0:128 offset1:160
	ds_read2_b32 v[146:147], v234 offset0:192 offset1:224
	s_waitcnt lgkmcnt(0)
	ds_read2_b32 v[148:149], v231 offset1:32
	ds_read2_b32 v[150:151], v231 offset0:64 offset1:96
	ds_read2_b32 v[152:153], v231 offset0:128 offset1:160
	ds_read2_b32 v[154:155], v231 offset0:192 offset1:224
	ds_read2_b32 v[156:157], v235 offset1:32
	ds_read2_b32 v[158:159], v235 offset0:64 offset1:96
	ds_read2_b32 v[160:161], v235 offset0:128 offset1:160
	ds_read2_b32 v[162:163], v235 offset0:192 offset1:224
	v_pk_mul_f32 v[132:133], v[132:133], v[214:215]
	v_pk_mul_f32 v[134:135], v[134:135], v[216:217]
	v_pk_mul_f32 v[136:137], v[136:137], v[218:219]
	v_pk_mul_f32 v[138:139], v[138:139], v[220:221]
	v_pk_mul_f32 v[140:141], v[140:141], v[222:223]
	v_pk_mul_f32 v[142:143], v[142:143], v[224:225]
	v_pk_mul_f32 v[144:145], v[144:145], v[226:227]
	v_pk_mul_f32 v[146:147], v[146:147], v[228:229]
	v_cvt_pk_fp8_f32 v244, v132, v133
	v_cvt_pk_fp8_f32 v245, v136, v137
	v_cvt_pk_fp8_f32 v246, v140, v141
	v_cvt_pk_fp8_f32 v247, v144, v145
	v_cvt_pk_fp8_f32 v244, v134, v135 op_sel:[0,0,1]
	v_cvt_pk_fp8_f32 v245, v138, v139 op_sel:[0,0,1]
	v_cvt_pk_fp8_f32 v246, v142, v143 op_sel:[0,0,1]
	v_cvt_pk_fp8_f32 v247, v146, v147 op_sel:[0,0,1]
	s_nop 0
	global_store_dwordx4 v238, v[244:247], s[46:47] nt
	s_waitcnt lgkmcnt(0)
	ds_read2_b32 v[164:165], v232 offset1:32
	ds_read2_b32 v[166:167], v232 offset0:64 offset1:96
	ds_read2_b32 v[168:169], v232 offset0:128 offset1:160
	ds_read2_b32 v[170:171], v232 offset0:192 offset1:224
	ds_read2_b32 v[172:173], v236 offset1:32
	ds_read2_b32 v[174:175], v236 offset0:64 offset1:96
	ds_read2_b32 v[176:177], v236 offset0:128 offset1:160
	ds_read2_b32 v[178:179], v236 offset0:192 offset1:224
	v_pk_mul_f32 v[148:149], v[148:149], v[214:215]
	v_pk_mul_f32 v[150:151], v[150:151], v[216:217]
	v_pk_mul_f32 v[152:153], v[152:153], v[218:219]
	v_pk_mul_f32 v[154:155], v[154:155], v[220:221]
	v_pk_mul_f32 v[156:157], v[156:157], v[222:223]
	v_pk_mul_f32 v[158:159], v[158:159], v[224:225]
	v_pk_mul_f32 v[160:161], v[160:161], v[226:227]
	v_pk_mul_f32 v[162:163], v[162:163], v[228:229]
	v_cvt_pk_fp8_f32 v244, v148, v149
	v_cvt_pk_fp8_f32 v245, v152, v153
	v_cvt_pk_fp8_f32 v246, v156, v157
	v_cvt_pk_fp8_f32 v247, v160, v161
	v_cvt_pk_fp8_f32 v244, v150, v151 op_sel:[0,0,1]
	v_cvt_pk_fp8_f32 v245, v154, v155 op_sel:[0,0,1]
	v_cvt_pk_fp8_f32 v246, v158, v159 op_sel:[0,0,1]
	v_cvt_pk_fp8_f32 v247, v162, v163 op_sel:[0,0,1]
	s_nop 0
	global_store_dwordx4 v239, v[244:247], s[46:47] nt
	s_waitcnt lgkmcnt(0)
	ds_read2_b32 v[180:181], v233 offset1:32
	ds_read2_b32 v[182:183], v233 offset0:64 offset1:96
	ds_read2_b32 v[184:185], v233 offset0:128 offset1:160
	ds_read2_b32 v[186:187], v233 offset0:192 offset1:224
	ds_read2_b32 v[188:189], v237 offset1:32
	ds_read2_b32 v[190:191], v237 offset0:64 offset1:96
	ds_read2_b32 v[192:193], v237 offset0:128 offset1:160
	ds_read2_b32 v[194:195], v237 offset0:192 offset1:224
	v_pk_mul_f32 v[164:165], v[164:165], v[214:215]
	v_pk_mul_f32 v[166:167], v[166:167], v[216:217]
	v_pk_mul_f32 v[168:169], v[168:169], v[218:219]
	v_pk_mul_f32 v[170:171], v[170:171], v[220:221]
	v_pk_mul_f32 v[172:173], v[172:173], v[222:223]
	v_pk_mul_f32 v[174:175], v[174:175], v[224:225]
	v_pk_mul_f32 v[176:177], v[176:177], v[226:227]
	v_pk_mul_f32 v[178:179], v[178:179], v[228:229]
	v_cvt_pk_fp8_f32 v244, v164, v165
	v_cvt_pk_fp8_f32 v245, v168, v169
	v_cvt_pk_fp8_f32 v246, v172, v173
	v_cvt_pk_fp8_f32 v247, v176, v177
	v_cvt_pk_fp8_f32 v244, v166, v167 op_sel:[0,0,1]
	v_cvt_pk_fp8_f32 v245, v170, v171 op_sel:[0,0,1]
	v_cvt_pk_fp8_f32 v246, v174, v175 op_sel:[0,0,1]
	v_cvt_pk_fp8_f32 v247, v178, v179 op_sel:[0,0,1]
	s_nop 0
	global_store_dwordx4 v240, v[244:247], s[46:47] nt
	s_waitcnt lgkmcnt(0)
	v_pk_mul_f32 v[180:181], v[180:181], v[214:215]
	v_pk_mul_f32 v[182:183], v[182:183], v[216:217]
	v_pk_mul_f32 v[184:185], v[184:185], v[218:219]
	v_pk_mul_f32 v[186:187], v[186:187], v[220:221]
	v_pk_mul_f32 v[188:189], v[188:189], v[222:223]
	v_pk_mul_f32 v[190:191], v[190:191], v[224:225]
	v_pk_mul_f32 v[192:193], v[192:193], v[226:227]
	v_pk_mul_f32 v[194:195], v[194:195], v[228:229]
	v_cvt_pk_fp8_f32 v244, v180, v181
	v_cvt_pk_fp8_f32 v245, v184, v185
	v_cvt_pk_fp8_f32 v246, v188, v189
	v_cvt_pk_fp8_f32 v247, v192, v193
	v_cvt_pk_fp8_f32 v244, v182, v183 op_sel:[0,0,1]
	v_cvt_pk_fp8_f32 v245, v186, v187 op_sel:[0,0,1]
	v_cvt_pk_fp8_f32 v246, v190, v191 op_sel:[0,0,1]
	v_cvt_pk_fp8_f32 v247, v194, v195 op_sel:[0,0,1]
	s_nop 0
	global_store_dwordx4 v241, v[244:247], s[46:47] nt
	s_mov_b32 s62, 0
	s_add_i32 s4, s4, s60
	s_cmp_lt_u32 s4, s6
	s_cbranch_scc1 .Lhlp_loop

; #define RT_MMA(X, W) do { _Pragma("unroll") for (int q = 0; q < 4; ++q) _Pragma("unroll") for (int jj = 0; jj < 4; ++jj) { acc = __builtin_amdgcn_mfma_f32_32x32x2f32(W[q][jj], X[q][jj], acc, 0, 0, 0); ss += X[q][jj] * X[q][jj]; } } while (0)
; __device__ __forceinline__ void p8_router(const P& p, LAS unsigned char* lds, int bx, int G, int tid, int lane, int wave) {
;     ...
;             RT_LOAD(xa, wa, m0);
; #pragma unroll 1
;             for (int m = m0; m < m0 + 32; m += 2) {
;                 RT_LOAD(xb, wb, m + 1);
;                 RT_MMA(xa, wa);
;                 if (m + 2 < m0 + 32) RT_LOAD(xa, wa, m + 2);
;                 RT_MMA(xb, wb);
;             }
.LBB5_1469:
	s_waitcnt vmcnt(0)
	v_mfma_f32_32x32x2_f32 v[2:17], v62, v34, v[2:17]
	s_add_i32 s38, s8, -8
	v_lshl_add_u64 v[86:87], s[38:39], 4, v[94:95]
	global_load_dwordx4 v[70:73], v[116:117], off offset:-48
	global_load_dwordx4 v[78:81], v[116:117], off offset:-64
	global_load_dwordx4 v[66:69], v[86:87], off offset:48
	global_load_dwordx4 v[74:77], v[86:87], off offset:32
	global_load_dwordx4 v[82:85], v[86:87], off offset:16
	s_nop 0
	global_load_dwordx4 v[86:89], v[86:87], off
	s_cmp_ge_u32 s50, s58
	s_cselect_b64 s[48:49], -1, 0
	s_and_b64 vcc, exec, s[48:49]
	v_mfma_f32_32x32x2_f32 v[2:17], v63, v35, v[2:17]
	v_mfma_f32_32x32x2_f32 v[2:17], v64, v36, v[2:17]
	v_mfma_f32_32x32x2_f32 v[2:17], v65, v37, v[2:17]
	v_mfma_f32_32x32x2_f32 v[2:17], v58, v38, v[2:17]
	v_mfma_f32_32x32x2_f32 v[2:17], v59, v39, v[2:17]
	v_mfma_f32_32x32x2_f32 v[2:17], v60, v40, v[2:17]
	v_mfma_f32_32x32x2_f32 v[2:17], v61, v41, v[2:17]
	v_mfma_f32_32x32x2_f32 v[2:17], v54, v42, v[2:17]
	v_mfma_f32_32x32x2_f32 v[2:17], v55, v43, v[2:17]
	v_mfma_f32_32x32x2_f32 v[2:17], v56, v44, v[2:17]
	v_mfma_f32_32x32x2_f32 v[2:17], v57, v45, v[2:17]
	v_mfma_f32_32x32x2_f32 v[2:17], v50, v46, v[2:17]
	v_mfma_f32_32x32x2_f32 v[2:17], v51, v47, v[2:17]
	v_mfma_f32_32x32x2_f32 v[2:17], v52, v48, v[2:17]
	v_mfma_f32_32x32x2_f32 v[2:17], v53, v49, v[2:17]
	s_cbranch_vccnz .Lrt_skip
	s_mov_b32 s9, s39
	v_lshl_add_u64 v[18:19], s[8:9], 4, v[94:95]
	global_load_dwordx4 v[22:25], v[116:117], off
	global_load_dwordx4 v[30:33], v[116:117], off offset:16
	global_load_dwordx4 v[50:53], v[18:19], off offset:48
	global_load_dwordx4 v[54:57], v[18:19], off offset:32
	global_load_dwordx4 v[58:61], v[18:19], off offset:16
	global_load_dwordx4 v[62:65], v[18:19], off
	s_waitcnt vmcnt(6)
.LBB5_1471:
	v_lshlrev_b32_e32 v105, 16, v78
	v_fmac_f32_e32 v109, v34, v34
	v_fmac_f32_e32 v109, v35, v35
	v_mfma_f32_32x32x2_f32 v[2:17], v86, v105, v[2:17]
	v_and_b32_e32 v86, 0xffff0000, v78
	v_and_b32_e32 v78, 0xffff0000, v80
	v_fmac_f32_e32 v109, v36, v36
	v_fmac_f32_e32 v109, v37, v37
	v_fmac_f32_e32 v109, v38, v38
	v_fmac_f32_e32 v109, v39, v39
	v_fmac_f32_e32 v109, v40, v40
	v_fmac_f32_e32 v109, v41, v41
	v_fmac_f32_e32 v109, v42, v42
	v_fmac_f32_e32 v109, v43, v43
	v_fmac_f32_e32 v109, v44, v44
	v_fmac_f32_e32 v109, v45, v45
	v_fmac_f32_e32 v109, v46, v46
	v_fmac_f32_e32 v109, v47, v47
	v_fmac_f32_e32 v109, v48, v48
	v_mfma_f32_32x32x2_f32 v[2:17], v87, v86, v[2:17]
	v_lshlrev_b32_e32 v87, 16, v79
	v_fmac_f32_e32 v109, v49, v49
	v_fmac_f32_e32 v109, v105, v105
	v_fmac_f32_e32 v109, v86, v86
	v_fmac_f32_e32 v109, v87, v87
	s_add_i32 s50, s50, 2
	s_add_i32 s8, s8, 16
	v_lshl_add_u64 v[116:117], v[116:117], 0, s[16:17]
	s_and_b64 vcc, exec, s[48:49]
	v_mfma_f32_32x32x2_f32 v[2:17], v88, v87, v[2:17]
	v_and_b32_e32 v88, 0xffff0000, v79
	v_lshlrev_b32_e32 v79, 16, v80
	v_and_b32_e32 v80, 0xffff0000, v70
	v_fmac_f32_e32 v109, v88, v88
	v_mul_f32_e64 v34, v78, v78
	v_mul_f32_e64 v35, v79, v79
	v_add_f32_e32 v35, v35, v109
	v_add_f32_e32 v36, v34, v35
	v_mfma_f32_32x32x2_f32 v[2:17], v89, v88, v[2:17]
	v_mfma_f32_32x32x2_f32 v[2:17], v82, v79, v[2:17]
	v_and_b32_e32 v82, 0xffff0000, v81
	v_mfma_f32_32x32x2_f32 v[2:17], v83, v78, v[2:17]
	v_lshlrev_b32_e32 v83, 16, v81
	v_lshlrev_b32_e32 v81, 16, v70
	v_and_b32_e32 v70, 0xffff0000, v72
	v_mul_f32_e64 v34, v82, v82
	v_mul_f32_e64 v35, v83, v83
	v_add_f32_e32 v35, v35, v36
	v_add_f32_e32 v36, v34, v35
	v_mul_f32_e64 v34, v80, v80
	v_mul_f32_e64 v35, v81, v81
	v_add_f32_e32 v35, v35, v36
	v_add_f32_e32 v36, v34, v35
	v_mfma_f32_32x32x2_f32 v[2:17], v84, v83, v[2:17]
	v_mfma_f32_32x32x2_f32 v[2:17], v85, v82, v[2:17]
	v_mfma_f32_32x32x2_f32 v[2:17], v74, v81, v[2:17]
	v_and_b32_e32 v74, 0xffff0000, v71
	v_mfma_f32_32x32x2_f32 v[2:17], v75, v80, v[2:17]
	v_lshlrev_b32_e32 v75, 16, v71
	v_lshlrev_b32_e32 v71, 16, v72
	v_and_b32_e32 v72, 0xffff0000, v73
	v_lshlrev_b32_e32 v73, 16, v73
	v_mul_f32_e64 v34, v74, v74
	v_mul_f32_e64 v35, v75, v75
	v_add_f32_e32 v35, v35, v36
	v_add_f32_e32 v36, v34, v35
	v_mul_f32_e64 v34, v70, v70
	v_mul_f32_e64 v35, v71, v71
	v_add_f32_e32 v35, v35, v36
	v_add_f32_e32 v36, v34, v35
	v_mul_f32_e64 v34, v72, v72
	v_mul_f32_e64 v35, v73, v73
	v_add_f32_e32 v35, v35, v36
	v_mfma_f32_32x32x2_f32 v[2:17], v76, v75, v[2:17]
	v_add_f32_e32 v109, v34, v35
	v_mfma_f32_32x32x2_f32 v[2:17], v77, v74, v[2:17]
	v_mfma_f32_32x32x2_f32 v[2:17], v66, v71, v[2:17]
	v_mfma_f32_32x32x2_f32 v[2:17], v67, v70, v[2:17]
	v_mfma_f32_32x32x2_f32 v[2:17], v68, v73, v[2:17]
	v_mfma_f32_32x32x2_f32 v[2:17], v69, v72, v[2:17]
	s_cbranch_vccnz .LBB5_1473
	s_waitcnt vmcnt(5)
	v_lshlrev_b32_e32 v18, 16, v22
	v_and_b32_e32 v19, 0xffff0000, v22
	v_lshlrev_b32_e32 v20, 16, v23
	v_and_b32_e32 v21, 0xffff0000, v23
	v_lshlrev_b32_e32 v22, 16, v24
	v_and_b32_e32 v23, 0xffff0000, v24
	v_lshlrev_b32_e32 v24, 16, v25
	v_and_b32_e32 v25, 0xffff0000, v25
	s_waitcnt vmcnt(4)
	v_lshlrev_b32_e32 v26, 16, v30
	v_and_b32_e32 v27, 0xffff0000, v30
	v_lshlrev_b32_e32 v28, 16, v31
	v_and_b32_e32 v29, 0xffff0000, v31
	v_lshlrev_b32_e32 v30, 16, v32
	v_and_b32_e32 v31, 0xffff0000, v32
	v_lshlrev_b32_e32 v32, 16, v33
	v_and_b32_e32 v33, 0xffff0000, v33
	v_mov_b64_e32 v[48:49], v[32:33]
	v_mov_b64_e32 v[46:47], v[30:31]
	v_mov_b64_e32 v[44:45], v[28:29]
	v_mov_b64_e32 v[42:43], v[26:27]
	v_mov_b64_e32 v[40:41], v[24:25]
	v_mov_b64_e32 v[38:39], v[22:23]
	v_mov_b64_e32 v[36:37], v[20:21]
	v_mov_b64_e32 v[34:35], v[18:19]
	s_branch .LBB5_1469
.Lrt_skip:
	s_waitcnt vmcnt(0)
	s_branch .LBB5_1471
